# rwkv step 2b segment prefix and step 3 previous-row decay reads issued together instead of eight exec-masked blocks with a full LDS drain each
# speedup vs baseline: 1.0074x; 1.0008x over previous
.LBB0_395:
	s_waitcnt vmcnt(2)
	v_and_b32_e32 v33, 0xffff0000, v59
	v_and_b32_e32 v35, 0xffff0000, v55
	v_lshlrev_b32_e32 v34, 16, v38
	v_and_b32_e32 v32, 0xffff0000, v38
	v_lshlrev_b32_e32 v30, 16, v39
	v_and_b32_e32 v28, 0xffff0000, v39
	v_cndmask_b32_e64 v39, 0, v33, s[10:11]
	v_cndmask_b32_e64 v38, 0, v35, s[8:9]
	v_lshlrev_b32_e32 v33, 16, v52
	v_lshlrev_b32_e32 v35, 16, v56
	v_cndmask_b32_e64 v149, 0, v35, s[10:11]
	v_cndmask_b32_e64 v148, 0, v33, s[8:9]
	v_and_b32_e32 v33, 0xffff0000, v56
	v_and_b32_e32 v35, 0xffff0000, v52
	v_cndmask_b32_e64 v151, 0, v33, s[10:11]
	v_cndmask_b32_e64 v150, 0, v35, s[8:9]
	v_lshlrev_b32_e32 v33, 16, v53
	v_lshlrev_b32_e32 v35, 16, v57
	v_cndmask_b32_e64 v153, 0, v35, s[10:11]
	v_cndmask_b32_e64 v152, 0, v33, s[8:9]
	v_and_b32_e32 v33, 0xffff0000, v57
	v_and_b32_e32 v35, 0xffff0000, v53
	v_cndmask_b32_e64 v53, 0, v33, s[10:11]
	v_cndmask_b32_e64 v52, 0, v35, s[8:9]
	v_lshlrev_b32_e32 v33, 16, v54
	v_lshlrev_b32_e32 v35, 16, v58
	v_cndmask_b32_e64 v57, 0, v35, s[10:11]
	v_cndmask_b32_e64 v56, 0, v33, s[8:9]
	v_and_b32_e32 v33, 0xffff0000, v58
	v_and_b32_e32 v35, 0xffff0000, v54
	v_cndmask_b32_e64 v155, 0, v33, s[10:11]
	v_cndmask_b32_e64 v154, 0, v35, s[8:9]
	v_lshlrev_b32_e32 v33, 16, v55
	v_lshlrev_b32_e32 v35, 16, v59
	v_cndmask_b32_e64 v55, 0, v35, s[10:11]
	v_cndmask_b32_e64 v54, 0, v33, s[8:9]
	s_waitcnt vmcnt(1)
	v_lshlrev_b32_e32 v33, 16, v44
	s_waitcnt vmcnt(0)
	v_lshlrev_b32_e32 v35, 16, v48
	v_cndmask_b32_e64 v59, 0, v35, s[10:11]
	v_cndmask_b32_e64 v58, 0, v33, s[8:9]
	v_and_b32_e32 v33, 0xffff0000, v48
	v_and_b32_e32 v35, 0xffff0000, v44
	v_cndmask_b32_e64 v157, 0, v33, s[10:11]
	v_cndmask_b32_e64 v156, 0, v35, s[8:9]
	v_lshlrev_b32_e32 v33, 16, v45
	v_lshlrev_b32_e32 v35, 16, v49
	v_cndmask_b32_e64 v159, 0, v35, s[10:11]
	v_cndmask_b32_e64 v158, 0, v33, s[8:9]
	v_and_b32_e32 v33, 0xffff0000, v49
	v_and_b32_e32 v35, 0xffff0000, v45
	v_cndmask_b32_e64 v45, 0, v33, s[10:11]
	v_cndmask_b32_e64 v44, 0, v35, s[8:9]
	v_lshlrev_b32_e32 v33, 16, v46
	v_lshlrev_b32_e32 v35, 16, v50
	v_cndmask_b32_e64 v49, 0, v35, s[10:11]
	v_cndmask_b32_e64 v48, 0, v33, s[8:9]
	v_and_b32_e32 v33, 0xffff0000, v50
	v_and_b32_e32 v35, 0xffff0000, v46
	v_cndmask_b32_e64 v161, 0, v33, s[10:11]
	v_cndmask_b32_e64 v160, 0, v35, s[8:9]
	v_lshlrev_b32_e32 v33, 16, v47
	v_lshlrev_b32_e32 v35, 16, v51
	v_lshlrev_b32_e32 v67, 2, v74
	v_cndmask_b32_e64 v163, 0, v35, s[10:11]
	v_cndmask_b32_e64 v162, 0, v33, s[8:9]
	v_and_b32_e32 v33, 0xffff0000, v51
	v_and_b32_e32 v35, 0xffff0000, v47
	v_add_u32_e32 v29, v117, v67
	v_lshlrev_b32_e32 v84, 16, v42
	v_and_b32_e32 v86, 0xffff0000, v42
	v_lshlrev_b32_e32 v60, 16, v36
	v_and_b32_e32 v42, 0xffff0000, v36
	v_and_b32_e32 v36, 0xffff0000, v37
	v_cndmask_b32_e64 v47, 0, v33, s[10:11]
	v_cndmask_b32_e64 v46, 0, v35, s[8:9]
	v_pk_add_f32 v[164:165], v[46:47], v[28:29] op_sel_hi:[1,0] neg_lo:[0,1] neg_hi:[0,1]
	v_pk_add_f32 v[174:175], v[44:45], v[36:37] op_sel_hi:[1,0] neg_lo:[0,1] neg_hi:[0,1]
	v_pk_add_f32 v[176:177], v[48:49], v[34:35] op_sel_hi:[1,0] neg_lo:[0,1] neg_hi:[0,1]
	ds_read_b128 v[44:47], v29
	ds_read_b128 v[48:51], v29 offset:256
	v_and_b32_e32 v78, 0xffff0000, v40
	v_pk_add_f32 v[150:151], v[150:151], v[78:79] op_sel_hi:[1,0] neg_lo:[0,1] neg_hi:[0,1]
	v_mul_lo_u32 v33, v142, s39
	s_waitcnt lgkmcnt(1)
	v_mov_b32_e32 v178, v44
	s_waitcnt lgkmcnt(0)
	v_mov_b32_e32 v179, v48
	v_mov_b32_e32 v48, v45
	v_pk_mul_f32 v[44:45], v[150:151], v[48:49]
	v_lshlrev_b32_e32 v80, 16, v41
	v_and_b32_e32 v82, 0xffff0000, v41
	v_lshlrev_b32_e32 v88, 16, v43
	v_add3_u32 v71, v111, v104, v33
	v_pk_add_f32 v[160:161], v[160:161], v[32:33] op_sel_hi:[1,0] neg_lo:[0,1] neg_hi:[0,1]
	v_add_f32_e32 v33, v44, v78
	v_pk_add_f32 v[152:153], v[152:153], v[80:81] op_sel_hi:[1,0] neg_lo:[0,1] neg_hi:[0,1]
	v_pk_add_f32 v[166:167], v[52:53], v[82:83] op_sel_hi:[1,0] neg_lo:[0,1] neg_hi:[0,1]
	v_pk_add_f32 v[168:169], v[56:57], v[84:85] op_sel_hi:[1,0] neg_lo:[0,1] neg_hi:[0,1]
	v_pk_add_f32 v[170:171], v[54:55], v[88:89] op_sel_hi:[1,0] neg_lo:[0,1] neg_hi:[0,1]
	v_pk_add_f32 v[172:173], v[58:59], v[60:61] op_sel_hi:[1,0] neg_lo:[0,1] neg_hi:[0,1]
	ds_read_b128 v[52:55], v29 offset:16
	ds_read_b128 v[56:59], v29 offset:272
	v_add_f32_e32 v33, v33, v45
	v_mov_b32_e32 v44, v46
	v_mov_b32_e32 v45, v50
	v_lshlrev_b32_e32 v76, 16, v40
	v_pk_mul_f32 v[44:45], v[152:153], v[44:45]
	v_pk_add_f32 v[148:149], v[148:149], v[76:77] op_sel_hi:[1,0] neg_lo:[0,1] neg_hi:[0,1]
	v_add_f32_e32 v35, v44, v80
	v_mov_b32_e32 v50, v47
	v_pk_mul_f32 v[148:149], v[148:149], v[178:179]
	v_add_f32_e32 v35, v35, v45
	v_pk_mul_f32 v[44:45], v[166:167], v[50:51]
	v_lshlrev_b32_e32 v40, 16, v37
	v_add_f32_e32 v29, v148, v76
	v_add_f32_e32 v37, v44, v82
	v_add_f32_e32 v29, v29, v149
	v_add_f32_e32 v37, v37, v45
	s_waitcnt lgkmcnt(1)
	v_mov_b32_e32 v44, v52
	s_waitcnt lgkmcnt(0)
	v_mov_b32_e32 v45, v56
	v_pk_mul_f32 v[44:45], v[168:169], v[44:45]
	v_add_f32_e32 v29, v29, v29
	v_pk_add_f32 v[154:155], v[154:155], v[86:87] op_sel_hi:[1,0] neg_lo:[0,1] neg_hi:[0,1]
	v_pk_add_f32 v[158:159], v[158:159], v[40:41] op_sel_hi:[1,0] neg_lo:[0,1] neg_hi:[0,1]
	v_add_f32_e32 v41, v44, v84
	v_mov_b32_e32 v56, v53
	v_mul_f32_e32 v29, 0x3fb8aa3b, v29
	v_add_f32_e32 v33, v33, v33
	v_add_f32_e32 v41, v41, v45
	v_pk_mul_f32 v[44:45], v[154:155], v[56:57]
	v_exp_f32_e32 v29, v29
	v_mul_f32_e32 v33, 0x3fb8aa3b, v33
	v_and_b32_e32 v90, 0xffff0000, v43
	v_pk_add_f32 v[156:157], v[156:157], v[42:43] op_sel_hi:[1,0] neg_lo:[0,1] neg_hi:[0,1]
	v_add_f32_e32 v43, v44, v86
	v_exp_f32_e32 v33, v33
	v_add_f32_e32 v43, v43, v45
	v_mov_b32_e32 v44, v54
	v_mov_b32_e32 v45, v58
	v_pk_mul_f32 v[44:45], v[170:171], v[44:45]
	v_add_f32_e32 v29, 1.0, v29
	v_add_f32_e32 v44, v44, v88
	v_add_f32_e32 v47, v44, v45
	v_rcp_f32_e32 v44, v29
	v_add_f32_e32 v29, 1.0, v33
	v_add_f32_e32 v33, v35, v35
	v_mul_f32_e32 v33, 0x3fb8aa3b, v33
	v_add_f32_e32 v35, v37, v37
	v_rcp_f32_e32 v45, v29
	v_exp_f32_e32 v33, v33
	v_mul_f32_e32 v35, 0x3fb8aa3b, v35
	v_pk_add_f32 v[38:39], v[38:39], v[90:91] op_sel_hi:[1,0] neg_lo:[0,1] neg_hi:[0,1]
	v_mov_b32_e32 v58, v55
	v_exp_f32_e32 v35, v35
	v_pk_mul_f32 v[38:39], v[38:39], v[58:59]
	v_add_f32_e32 v33, 1.0, v33
	v_add_f32_e32 v29, v38, v90
	v_add_f32_e32 v29, v29, v39
	v_pk_fma_f32 v[38:39], v[44:45], 2.0, 1.0 op_sel_hi:[1,0,0] neg_lo:[1,0,0] neg_hi:[1,0,0]
	v_add_f32_e32 v29, v29, v29
	v_cvt_pk_bf16_f32 v44, v38, v39
	v_rcp_f32_e32 v38, v33
	v_add_f32_e32 v33, 1.0, v35
	v_rcp_f32_e32 v39, v33
	v_add_f32_e32 v33, v41, v41
	v_mul_f32_e32 v33, 0x3fb8aa3b, v33
	v_add_f32_e32 v35, v43, v43
	v_exp_f32_e32 v33, v33
	v_mul_f32_e32 v35, 0x3fb8aa3b, v35
	v_exp_f32_e32 v35, v35
	v_mul_f32_e32 v29, 0x3fb8aa3b, v29
	v_add_f32_e32 v33, 1.0, v33
	v_rcp_f32_e32 v46, v33
	v_add_f32_e32 v33, 1.0, v35
	v_add_f32_e32 v35, v47, v47
	v_mul_f32_e32 v35, 0x3fb8aa3b, v35
	v_exp_f32_e32 v35, v35
	v_exp_f32_e32 v29, v29
	v_rcp_f32_e32 v47, v33
	v_pk_fma_f32 v[38:39], v[38:39], 2.0, 1.0 op_sel_hi:[1,0,0] neg_lo:[1,0,0] neg_hi:[1,0,0]
	v_add_f32_e32 v33, 1.0, v35
	v_add_f32_e32 v29, 1.0, v29
	v_rcp_f32_e32 v48, v33
	v_rcp_f32_e32 v49, v29
	v_cvt_pk_bf16_f32 v45, v38, v39
	v_pk_fma_f32 v[38:39], v[46:47], 2.0, 1.0 op_sel_hi:[1,0,0] neg_lo:[1,0,0] neg_hi:[1,0,0]
	v_add_u32_e32 v31, v118, v67
	v_cvt_pk_bf16_f32 v46, v38, v39
	v_pk_fma_f32 v[38:39], v[48:49], 2.0, 1.0 op_sel_hi:[1,0,0] neg_lo:[1,0,0] neg_hi:[1,0,0]
	s_lshl_b32 s0, s26, 10
	v_cvt_pk_bf16_f32 v47, v38, v39
	ds_write_b128 v71, v[44:47]
	ds_read_b128 v[44:47], v31
	ds_read_b128 v[48:51], v31 offset:256
	ds_read_b128 v[52:55], v31 offset:16
	ds_read_b128 v[56:59], v31 offset:272
	v_pk_add_f32 v[38:39], v[162:163], v[30:31] op_sel_hi:[1,0] neg_lo:[0,1] neg_hi:[0,1]
	s_or_b32 s28, s0, s5
	s_waitcnt lgkmcnt(3)
	v_mov_b32_e32 v76, v44
	s_waitcnt lgkmcnt(2)
	v_mov_b32_e32 v77, v48
	v_mov_b32_e32 v48, v45
	v_pk_mul_f32 v[44:45], v[156:157], v[48:49]
	v_mov_b32_e32 v43, v50
	v_add_f32_e32 v31, v44, v42
	v_mov_b32_e32 v42, v46
	v_pk_mul_f32 v[42:43], v[158:159], v[42:43]
	v_mov_b32_e32 v50, v47
	v_add_f32_e32 v44, v31, v45
	v_add_f32_e32 v31, v42, v40
	v_pk_mul_f32 v[40:41], v[174:175], v[50:51]
	v_add_f32_e32 v42, v31, v43
	v_add_f32_e32 v31, v40, v36
	s_waitcnt lgkmcnt(1)
	v_mov_b32_e32 v36, v52
	s_waitcnt lgkmcnt(0)
	v_mov_b32_e32 v37, v56
	v_pk_mul_f32 v[36:37], v[176:177], v[36:37]
	v_mov_b32_e32 v56, v53
	v_add_f32_e32 v40, v31, v41
	v_add_f32_e32 v31, v36, v34
	v_pk_mul_f32 v[34:35], v[160:161], v[56:57]
	v_add_f32_e32 v36, v31, v37
	v_add_f32_e32 v31, v34, v32
	v_mov_b32_e32 v32, v54
	v_mov_b32_e32 v33, v58
	v_pk_mul_f32 v[32:33], v[38:39], v[32:33]
	v_mov_b32_e32 v58, v55
	v_add_f32_e32 v30, v32, v30
	v_pk_mul_f32 v[76:77], v[172:173], v[76:77]
	v_add_f32_e32 v34, v31, v35
	v_add_f32_e32 v32, v30, v33
	v_pk_mul_f32 v[30:31], v[164:165], v[58:59]
	v_add_f32_e32 v29, v76, v60
	v_add_f32_e32 v28, v30, v28
	v_add_f32_e32 v29, v29, v77
	v_add_f32_e32 v31, v28, v31
	v_cvt_pk_bf16_f32 v28, v29, v44
	v_cvt_pk_bf16_f32 v29, v42, v40
	v_cvt_pk_bf16_f32 v30, v36, v34
	v_cvt_pk_bf16_f32 v31, v32, v31
	s_or_b32 s0, s41, s28
	s_mov_b32 s1, s29
	ds_write_b128 v71, v[28:31] offset:9216
	s_lshl_b64 s[0:1], s[0:1], 7
	v_and_b32_e32 v51, 15, v103
	v_lshrrev_b32_e32 v28, 1, v103
	s_add_u32 s60, s51, s0
	v_and_b32_e32 v50, 24, v28
	v_or_b32_e32 v48, s27, v51
	s_addc_u32 s61, s70, s1
	v_lshlrev_b32_e32 v44, 1, v50
	v_mov_b32_e32 v45, v105
	v_ashrrev_i32_e32 v49, 31, v48
	v_lshl_add_u64 v[28:29], s[60:61], 0, v[44:45]
	v_lshlrev_b64 v[30:31], 7, v[48:49]
	v_lshl_add_u64 v[32:33], v[28:29], 0, v[30:31]
	global_load_dwordx4 v[52:55], v[32:33], off
	global_load_dwordx4 v[56:59], v[32:33], off offset:64
	v_or_b32_e32 v49, s41, v51
	v_add_u32_e32 v32, s27, v49
	v_ashrrev_i32_e32 v33, 31, v32
	v_lshl_add_u64 v[32:33], v[32:33], 0, s[28:29]
	v_readlane_b32 s76, v253, 26
	v_lshlrev_b64 v[32:33], 2, v[32:33]
	v_readlane_b32 s90, v253, 40
	v_readlane_b32 s91, v253, 41
	s_add_u32 s0, s71, s0
	s_addc_u32 s1, s49, s1
	v_lshl_add_u64 v[34:35], s[90:91], 0, v[32:33]
	global_load_dword v60, v[34:35], off
	v_lshl_add_u64 v[34:35], s[0:1], 0, v[44:45]
	v_lshl_add_u64 v[30:31], v[34:35], 0, v[30:31]
	global_load_dwordx4 v[76:79], v[30:31], off
	global_load_dwordx4 v[80:83], v[30:31], off offset:64
	v_readlane_b32 s77, v253, 27
	v_readlane_b32 s78, v253, 28
	v_readlane_b32 s79, v253, 29
	v_readlane_b32 s80, v253, 30
	v_readlane_b32 s81, v253, 31
	v_readlane_b32 s82, v253, 32
	v_readlane_b32 s83, v253, 33
	v_readlane_b32 s84, v253, 34
	v_readlane_b32 s85, v253, 35
	v_readlane_b32 s86, v253, 36
	v_readlane_b32 s87, v253, 37
	v_readlane_b32 s72, v253, 42
	v_readlane_b32 s74, v253, 44
	v_readlane_b32 s75, v253, 45
	v_or_b32_e32 v46, s63, v51
	v_ashrrev_i32_e32 v47, 31, v46
	v_lshl_add_u64 v[30:31], s[74:75], 0, v[32:33]
	global_load_dword v71, v[30:31], off
	v_lshlrev_b64 v[30:31], 7, v[46:47]
	v_lshl_add_u64 v[28:29], v[28:29], 0, v[30:31]
	v_lshl_add_u64 v[30:31], v[34:35], 0, v[30:31]
	global_load_dwordx4 v[84:87], v[28:29], off
	global_load_dwordx4 v[88:91], v[28:29], off offset:64
	global_load_dwordx4 v[148:151], v[30:31], off
	global_load_dwordx4 v[152:155], v[30:31], off offset:64
	v_add_u32_e32 v156, s63, v49
	s_lshl_b32 s41, s41, 2
	v_ashrrev_i32_e32 v157, 31, v156
	v_or_b32_e32 v45, s34, v51
	s_add_u32 s0, s42, s41
	v_lshl_add_u64 v[156:157], v[156:157], 0, s[28:29]
	v_mul_u32_u24_e32 v45, 0x48, v45
	s_addc_u32 s1, s36, 0
	v_lshlrev_b64 v[156:157], 2, v[156:157]
	v_lshlrev_b32_e32 v45, 1, v45
	s_add_u32 s60, s52, s41
	v_lshl_add_u64 v[158:159], s[90:91], 0, v[156:157]
	v_lshl_add_u64 v[156:157], s[74:75], 0, v[156:157]
	v_add3_u32 v45, v111, v45, v44
	s_addc_u32 s61, s53, 0
	global_load_dwordx4 v[32:35], v67, s[0:1] offset:16
	global_load_dwordx4 v[40:43], v67, s[0:1]
	global_load_dwordx4 v[28:31], v67, s[60:61] offset:16
	global_load_dwordx4 v[36:39], v67, s[60:61]
	global_load_dword v75, v[156:157], off
	s_mov_b32 s0, 0xbfb8aa3b
	global_load_dword v67, v[158:159], off
	s_waitcnt lgkmcnt(0)
	s_barrier
	ds_read_b128 v[156:159], v45
	ds_read_b128 v[160:163], v45 offset:64
	s_waitcnt vmcnt(15) lgkmcnt(1)
	v_mfma_f32_16x16x32_bf16 v[52:55], v[156:159], v[52:55], 0
	ds_read_b128 v[164:167], v45 offset:9216
	s_movk_i32 s1, 0x41
	v_and_b32_e32 v49, 63, v103
	s_waitcnt vmcnt(14) lgkmcnt(1)
	v_mfma_f32_16x16x32_bf16 v[52:55], v[160:163], v[56:59], v[52:55]
	v_readlane_b32 s88, v253, 38
	v_readlane_b32 s89, v253, 39
	v_readlane_b32 s73, v253, 43
	v_readlane_b32 s76, v253, 46
	v_readlane_b32 s77, v253, 47
	v_readlane_b32 s78, v253, 48
	v_readlane_b32 s79, v253, 49
	v_readlane_b32 s80, v253, 50
	s_waitcnt vmcnt(13)
	v_add_f32_e32 v52, v60, v52
	v_mul_f32_e64 v47, |v52|, s0
	v_exp_f32_e32 v56, v47
	v_lshrrev_b32_e32 v47, 2, v103
	v_add_f32_e32 v53, v60, v53
	v_add_f32_e32 v54, v60, v54
	v_add_f32_e32 v56, 1.0, v56
	v_log_f32_e32 v147, v56
	ds_read_b128 v[56:59], v45 offset:9280
	s_waitcnt vmcnt(12) lgkmcnt(1)
	v_mfma_f32_16x16x32_bf16 v[76:79], v[164:167], v[76:79], 0
	v_max_f32_e64 v45, -v52, 0
	v_fmac_f32_e32 v45, 0x3f317218, v147
	v_sub_f32_e32 v45, -0.5, v45
	s_waitcnt vmcnt(11) lgkmcnt(0)
	v_mfma_f32_16x16x32_bf16 v[76:79], v[56:59], v[80:83], v[76:79]
	v_mul_f32_e32 v45, 0x3fb8aa3b, v45
	v_exp_f32_e32 v52, v45
	v_and_b32_e32 v45, 12, v47
	s_waitcnt vmcnt(10)
	s_nop 3
	v_add_f32_e32 v76, v71, v76
	v_mul_f32_e32 v76, 0xbfb8aa3b, v76
	v_exp_f32_e32 v76, v76
	v_or_b32_e32 v147, s34, v45
	v_mul_u32_u24_e32 v80, 0x41, v147
	v_add_lshl_u32 v81, v80, v48, 2
	v_add_f32_e32 v76, 1.0, v76
	v_rcp_f32_e32 v76, v76
	v_mul_f32_e64 v82, |v53|, s0
	v_xor_b32_e32 v52, 0x80000000, v52
	v_exp_f32_e32 v82, v82
	v_add_u32_e32 v83, v113, v81
	ds_write_b32 v83, v52
	v_add_u32_e32 v52, v119, v81
	ds_write_b32 v52, v76
	v_add_f32_e32 v76, v71, v77
	v_mul_f32_e64 v77, |v54|, s0
	v_exp_f32_e32 v77, v77
	v_add_f32_e32 v82, 1.0, v82
	v_log_f32_e32 v82, v82
	v_max_f32_e64 v53, -v53, 0
	v_add_f32_e32 v77, 1.0, v77
	v_log_f32_e32 v77, v77
	v_fmac_f32_e32 v53, 0x3f317218, v82
	v_mul_f32_e32 v76, 0xbfb8aa3b, v76
	v_sub_f32_e32 v53, -0.5, v53
	v_exp_f32_e32 v76, v76
	v_mul_f32_e32 v53, 0x3fb8aa3b, v53
	v_max_f32_e64 v54, -v54, 0
	v_exp_f32_e32 v53, v53
	v_fmac_f32_e32 v54, 0x3f317218, v77
	v_sub_f32_e32 v54, -0.5, v54
	v_add_f32_e32 v55, v60, v55
	v_add_f32_e32 v76, 1.0, v76
	v_mul_f32_e32 v54, 0x3fb8aa3b, v54
	v_mul_f32_e64 v60, |v55|, s0
	v_mad_u32_u24 v81, v147, s1, s1
	v_rcp_f32_e32 v76, v76
	v_exp_f32_e32 v54, v54
	v_exp_f32_e32 v60, v60
	v_xor_b32_e32 v52, 0x80000000, v53
	v_add_lshl_u32 v53, v81, v48, 2
	v_add_u32_e32 v82, v113, v53
	ds_write_b32 v82, v52
	v_add_u32_e32 v52, v119, v53
	ds_write_b32 v52, v76
	v_xor_b32_e32 v52, 0x80000000, v54
	v_add_f32_e32 v54, v71, v78
	v_add_f32_e32 v60, 1.0, v60
	v_mul_f32_e32 v54, 0xbfb8aa3b, v54
	v_log_f32_e32 v60, v60
	v_exp_f32_e32 v54, v54
	v_max_f32_e64 v55, -v55, 0
	v_mov_b32_e32 v53, 0x82
	v_fmac_f32_e32 v55, 0x3f317218, v60
	v_add_f32_e32 v54, 1.0, v54
	v_sub_f32_e32 v55, -0.5, v55
	v_mad_u32_u24 v82, v147, s1, v53
	v_rcp_f32_e32 v54, v54
	v_mul_f32_e32 v55, 0x3fb8aa3b, v55
	v_add_lshl_u32 v53, v82, v48, 2
	v_exp_f32_e32 v55, v55
	v_add_u32_e32 v76, v113, v53
	ds_write_b32 v76, v52
	v_add_u32_e32 v52, v119, v53
	ds_write_b32 v52, v54
	v_mov_b32_e32 v52, 0xc3
	v_xor_b32_e32 v60, 0x80000000, v55
	v_mad_u32_u24 v83, v147, s1, v52
	s_waitcnt vmcnt(9)
	v_mfma_f32_16x16x32_bf16 v[52:55], v[156:159], v[84:87], 0
	v_add_f32_e32 v71, v71, v79
	v_mul_f32_e32 v71, 0xbfb8aa3b, v71
	v_exp_f32_e32 v71, v71
	s_waitcnt vmcnt(8)
	v_mfma_f32_16x16x32_bf16 v[52:55], v[160:163], v[88:91], v[52:55]
	v_add_lshl_u32 v48, v83, v48, 2
	v_add_u32_e32 v76, v113, v48
	ds_write_b32 v76, v60
	v_add_f32_e32 v60, 1.0, v71
	v_rcp_f32_e32 v60, v60
	s_waitcnt vmcnt(0)
	s_nop 1
	v_add_f32_e32 v52, v67, v52
	v_mul_f32_e64 v77, |v52|, s0
	v_exp_f32_e32 v77, v77
	v_add_u32_e32 v48, v119, v48
	v_add_f32_e32 v53, v67, v53
	v_max_f32_e64 v52, -v52, 0
	v_add_f32_e32 v71, 1.0, v77
	v_mfma_f32_16x16x32_bf16 v[76:79], v[164:167], v[148:151], 0
	v_log_f32_e32 v71, v71
	ds_write_b32 v48, v60
	v_mul_f32_e64 v60, |v53|, s0
	v_mfma_f32_16x16x32_bf16 v[56:59], v[56:59], v[152:155], v[76:79]
	v_fmac_f32_e32 v52, 0x3f317218, v71
	v_exp_f32_e32 v60, v60
	v_sub_f32_e32 v52, -0.5, v52
	v_mul_f32_e32 v52, 0x3fb8aa3b, v52
	v_exp_f32_e32 v52, v52
	s_nop 2
	v_add_f32_e32 v56, v75, v56
	v_mul_f32_e32 v56, 0xbfb8aa3b, v56
	v_exp_f32_e32 v56, v56
	v_add_f32_e32 v60, 1.0, v60
	v_log_f32_e32 v60, v60
	v_xor_b32_e32 v48, 0x80000000, v52
	v_add_f32_e32 v56, 1.0, v56
	v_rcp_f32_e32 v56, v56
	v_add_lshl_u32 v52, v80, v46, 2
	v_add_u32_e32 v71, v113, v52
	v_max_f32_e64 v53, -v53, 0
	v_fmac_f32_e32 v53, 0x3f317218, v60
	ds_write_b32 v71, v48
	v_add_u32_e32 v48, v119, v52
	v_add_f32_e32 v54, v67, v54
	v_sub_f32_e32 v53, -0.5, v53
	ds_write_b32 v48, v56
	v_mul_f32_e64 v56, |v54|, s0
	v_mul_f32_e32 v53, 0x3fb8aa3b, v53
	v_exp_f32_e32 v56, v56
	v_exp_f32_e32 v53, v53
	v_max_f32_e64 v54, -v54, 0
	v_add_lshl_u32 v52, v81, v46, 2
	v_add_f32_e32 v56, 1.0, v56
	v_xor_b32_e32 v48, 0x80000000, v53
	v_add_f32_e32 v53, v75, v57
	v_log_f32_e32 v56, v56
	v_mul_f32_e32 v53, 0xbfb8aa3b, v53
	v_exp_f32_e32 v53, v53
	v_add_u32_e32 v57, v113, v52
	v_fmac_f32_e32 v54, 0x3f317218, v56
	v_sub_f32_e32 v54, -0.5, v54
	v_add_f32_e32 v53, 1.0, v53
	v_mul_f32_e32 v54, 0x3fb8aa3b, v54
	v_rcp_f32_e32 v53, v53
	v_exp_f32_e32 v54, v54
	ds_write_b32 v57, v48
	v_add_u32_e32 v48, v119, v52
	ds_write_b32 v48, v53
	v_xor_b32_e32 v48, 0x80000000, v54
	v_add_f32_e32 v53, v75, v58
	v_add_f32_e32 v54, v67, v55
	v_mul_f32_e32 v53, 0xbfb8aa3b, v53
	v_mul_f32_e64 v55, |v54|, s0
	v_exp_f32_e32 v53, v53
	v_exp_f32_e32 v55, v55
	v_add_lshl_u32 v52, v82, v46, 2
	v_add_u32_e32 v56, v113, v52
	ds_write_b32 v56, v48
	v_add_f32_e32 v48, 1.0, v53
	v_add_f32_e32 v53, 1.0, v55
	v_log_f32_e32 v53, v53
	v_max_f32_e64 v54, -v54, 0
	v_rcp_f32_e32 v48, v48
	v_add_u32_e32 v52, v119, v52
	v_fmac_f32_e32 v54, 0x3f317218, v53
	v_sub_f32_e32 v53, -0.5, v54
	v_mul_f32_e32 v53, 0x3fb8aa3b, v53
	v_exp_f32_e32 v53, v53
	v_add_f32_e32 v54, v75, v59
	v_mul_f32_e32 v54, 0xbfb8aa3b, v54
	v_add_lshl_u32 v46, v83, v46, 2
	v_exp_f32_e32 v54, v54
	ds_write_b32 v52, v48
	v_xor_b32_e32 v48, 0x80000000, v53
	v_add_u32_e32 v53, v113, v46
	ds_write_b32 v53, v48
	v_ashrrev_i32_e32 v48, 6, v103
	v_lshlrev_b32_e32 v59, 3, v48
	v_or_b32_e32 v53, 1, v59
	v_add_f32_e32 v52, 1.0, v54
	v_sub_u32_e32 v54, 63, v53
	v_cndmask_b32_e64 v53, v54, v53, s[12:13]
	v_or_b32_e32 v54, 2, v59
	v_sub_u32_e32 v55, 63, v54
	v_cndmask_b32_e64 v54, v55, v54, s[12:13]
	v_or_b32_e32 v55, 3, v59
	v_sub_u32_e32 v56, 63, v55
	v_rcp_f32_e32 v52, v52
	v_cndmask_b32_e64 v55, v56, v55, s[12:13]
	v_or_b32_e32 v56, 4, v59
	v_sub_u32_e32 v57, 63, v56
	v_cndmask_b32_e64 v56, v57, v56, s[12:13]
	v_or_b32_e32 v57, 5, v59
	v_add_u32_e32 v46, v119, v46
	v_sub_u32_e32 v58, 63, v57
	ds_write_b32 v46, v52
	v_sub_u32_e32 v52, 63, v59
	v_cndmask_b32_e64 v57, v58, v57, s[12:13]
	v_or_b32_e32 v58, 6, v59
	v_cndmask_b32_e64 v52, v52, v59, s[12:13]
	v_sub_u32_e32 v67, 63, v58
	v_or_b32_e32 v59, 7, v59
	v_lshlrev_b32_e32 v46, 2, v49
	s_movk_i32 s0, 0x104
	v_cndmask_b32_e64 v58, v67, v58, s[12:13]
	v_sub_u32_e32 v67, 63, v59
	v_add_u32_e32 v60, v113, v46
	v_mul_lo_u32 v52, v52, s0
	v_cndmask_b32_e64 v59, v67, v59, s[12:13]
	v_add_u32_e32 v52, v60, v52
	v_mul_lo_u32 v53, v53, s0
	v_mul_lo_u32 v54, v54, s0
	v_mul_lo_u32 v55, v55, s0
	v_mul_lo_u32 v56, v56, s0
	v_mul_lo_u32 v57, v57, s0
	v_mul_lo_u32 v58, v58, s0
	v_mul_lo_u32 v59, v59, s0
	s_waitcnt lgkmcnt(0)
	s_barrier
	v_add_u32_e32 v53, v60, v53
	v_add_u32_e32 v54, v60, v54
	v_add_u32_e32 v55, v60, v55
	v_add_u32_e32 v56, v60, v56
	v_add_u32_e32 v57, v60, v57
	v_add_u32_e32 v58, v60, v58
	v_add_u32_e32 v59, v60, v59
	ds_read_b32 v60, v52
	ds_read_b32 v67, v53
	ds_read_b32 v71, v54
	ds_read_b32 v75, v55
	ds_read_b32 v80, v56
	ds_read_b32 v81, v57
	ds_read_b32 v82, v58
	ds_read_b32 v83, v59
	s_waitcnt lgkmcnt(7)
	v_add_f32_e32 v79, 0, v60
	s_waitcnt lgkmcnt(6)
	v_add_f32_e32 v78, v79, v67
	s_waitcnt lgkmcnt(5)
	v_add_f32_e32 v77, v78, v71
	s_waitcnt lgkmcnt(4)
	v_add_f32_e32 v76, v77, v75
	s_waitcnt lgkmcnt(3)
	v_add_f32_e32 v75, v76, v80
	s_waitcnt lgkmcnt(2)
	v_add_f32_e32 v71, v75, v81
	s_waitcnt lgkmcnt(1)
	v_add_f32_e32 v67, v71, v82
	s_waitcnt lgkmcnt(0)
	v_add_f32_e32 v60, v67, v83
	v_lshl_add_u32 v80, v103, 2, v120
	ds_write_b32 v80, v60
	v_add_u32_e32 v81, v120, v46
	v_cmp_lt_i32_e32 vcc, 0, v48
	v_mov_b32_e32 v80, 0
	v_readlane_b32 s81, v253, 51
	v_readlane_b32 s82, v253, 52
	v_readlane_b32 s83, v253, 53
	v_readlane_b32 s84, v253, 54
	v_readlane_b32 s85, v253, 55
	v_readlane_b32 s86, v253, 56
	v_readlane_b32 s87, v253, 57
	s_waitcnt lgkmcnt(0)
	s_barrier
	ds_read_b32 v216, v81
	ds_read_b32 v217, v81 offset:256
	ds_read_b32 v218, v81 offset:512
	ds_read_b32 v219, v81 offset:768
	ds_read_b32 v220, v81 offset:1024
	ds_read_b32 v221, v81 offset:1280
	ds_read_b32 v222, v81 offset:1536
	v_readfirstlane_b32 s0, v48
	s_movk_i32 s75, 0xfc0
	s_waitcnt lgkmcnt(0)
	s_cmp_lt_i32 s0, 1
	s_cbranch_scc1 .Lseg_done
	v_add_f32_e32 v80, 0, v216
	s_cmp_lt_i32 s0, 2
	s_cbranch_scc1 .Lseg_done
	v_add_f32_e32 v80, v80, v217
	s_cmp_lt_i32 s0, 3
	s_cbranch_scc1 .Lseg_done
	v_add_f32_e32 v80, v80, v218
	s_cmp_lt_i32 s0, 4
	s_cbranch_scc1 .Lseg_done
	v_add_f32_e32 v80, v80, v219
	s_cmp_lt_i32 s0, 5
	s_cbranch_scc1 .Lseg_done
	v_add_f32_e32 v80, v80, v220
	s_cmp_lt_i32 s0, 6
	s_cbranch_scc1 .Lseg_done
	v_add_f32_e32 v80, v80, v221
	s_cmp_lt_i32 s0, 7
	s_cbranch_scc1 .Lseg_done
	v_add_f32_e32 v80, v80, v222
.Lseg_done:
	v_add_f32_e32 v79, v79, v80
	ds_write_b32 v52, v79
	v_add_f32_e32 v52, v78, v80
	ds_write_b32 v53, v52
	v_add_f32_e32 v52, v77, v80
	ds_write_b32 v54, v52
	v_add_f32_e32 v52, v76, v80
	ds_write_b32 v55, v52
	v_add_f32_e32 v52, v75, v80
	ds_write_b32 v56, v52
	v_add_f32_e32 v52, v71, v80
	ds_write_b32 v57, v52
	v_add_f32_e32 v52, v67, v80
	ds_write_b32 v58, v52
	v_add_f32_e32 v52, v60, v80
	v_cmp_eq_u32_e32 vcc, 7, v48
	ds_write_b32 v59, v52
	s_and_saveexec_b64 s[0:1], vcc
	s_cbranch_execz .LBB0_408
	v_mul_f32_e32 v48, 0x3fb8aa3b, v52
	v_exp_f32_e32 v48, v48
	v_lshl_add_u32 v52, v49, 2, v114
	ds_write_b32 v52, v48
.LBB0_408:
	s_or_b64 exec, exec, s[0:1]
	v_lshl_add_u32 v52, v142, 6, v142
	v_lshl_add_u32 v55, v74, 2, v113
	v_lshl_add_u32 v60, v52, 2, v55
	s_waitcnt lgkmcnt(0)
	s_barrier
	s_and_b64 s[0:1], exec, s[12:13]
	ds_read_b32 v54, v60
	s_cselect_b32 s0, -1, 1
	v_sub_u32_e32 v48, 63, v142
	v_add_u32_e32 v53, s0, v142
	s_movk_i32 s0, 0x104
	v_cndmask_b32_e64 v48, v48, v142, s[12:13]
	v_mul_lo_u32 v56, v53, s0
	v_cmp_lt_i32_e32 vcc, 0, v48
	v_mov_b32_e32 v53, 0
	v_add_u32_e32 v87, v55, v56
	v_mov_b32_e32 v56, 0
	v_mov_b32_e32 v224, 0x3fb8aa3b
	v_cndmask_b32_e32 v87, v60, v87, vcc
	v_cndmask_b32_e32 v224, 0, v224, vcc
	ds_read_b32 v216, v87
	ds_read_b32 v217, v87 offset:4
	ds_read_b32 v218, v87 offset:8
	ds_read_b32 v219, v87 offset:12
	ds_read_b32 v220, v87 offset:16
	ds_read_b32 v221, v87 offset:20
	ds_read_b32 v222, v87 offset:24
	ds_read_b32 v223, v87 offset:28
	v_add_u32_e32 v52, v52, v74
	v_lshl_add_u32 v52, v52, 2, v119
	ds_read_b32 v57, v52
	ds_read_b32 v55, v60 offset:4
	ds_read_b32 v58, v52 offset:4
	ds_read_b32 v71, v60 offset:8
	ds_read_b32 v76, v52 offset:8
	ds_read_b32 v74, v60 offset:12
	s_waitcnt lgkmcnt(6)
	v_mul_f32_e32 v56, v224, v216
	v_mul_f32_e32 v53, v224, v217
	v_mul_f32_e32 v75, v224, v218
	v_mul_f32_e32 v67, v224, v219
	v_mul_f32_e32 v81, v224, v220
	v_mul_f32_e32 v78, v224, v221
	v_mul_f32_e32 v85, v224, v222
	v_mul_f32_e32 v59, v224, v223
	ds_read_b32 v77, v52 offset:12
	ds_read_b32 v79, v60 offset:16
	ds_read_b32 v82, v52 offset:16
	ds_read_b32 v80, v60 offset:20
	ds_read_b32 v83, v52 offset:20
	ds_read_b32 v84, v60 offset:24
	ds_read_b32 v86, v52 offset:24
	ds_read_b32 v60, v60 offset:28
	v_lshlrev_b32_e32 v88, 16, v16
	v_lshlrev_b32_e32 v87, 16, v8
	v_cndmask_b32_e64 v88, 0, v88, s[8:9]
	v_lshlrev_b32_e32 v89, 16, v12
	v_cndmask_b32_e64 v89, 0, v89, s[10:11]
	v_sub_f32_e32 v88, v88, v87
	v_and_b32_e32 v16, 0xffff0000, v16
	v_sub_f32_e32 v89, v89, v87
	v_fmac_f32_e32 v87, v88, v20
	v_add_f32_e32 v20, v62, v63
	v_and_b32_e32 v8, 0xffff0000, v8
	v_cndmask_b32_e64 v16, 0, v16, s[8:9]
	v_and_b32_e32 v12, 0xffff0000, v12
	v_max_f32_e32 v20, 0x179abe15, v20
	v_cndmask_b32_e64 v12, 0, v12, s[10:11]
	v_sub_f32_e32 v16, v16, v8
	v_fmac_f32_e32 v87, v89, v24
	v_rsq_f32_e32 v24, v20
	s_waitcnt lgkmcnt(13)
	v_add_f32_e32 v20, -1.0, v57
	v_sub_f32_e32 v12, v12, v8
	v_fmac_f32_e32 v8, v16, v21
	v_fma_f32 v20, v40, v20, 1.0
	v_fmac_f32_e32 v8, v12, v25
	s_waitcnt lgkmcnt(11)
	v_add_f32_e32 v12, -1.0, v58
	v_mul_f32_e32 v20, v146, v20
	v_fma_f32 v12, v41, v12, 1.0
	v_mul_f32_e32 v40, v87, v20
	v_mul_f32_e32 v12, v145, v12
	v_fma_f32 v36, v36, v40, 0
	v_mul_f32_e32 v16, v8, v12
	v_lshlrev_b32_e32 v21, 16, v17
	v_and_b32_e32 v17, 0xffff0000, v17
	v_fmac_f32_e32 v36, v37, v16
	v_lshlrev_b32_e32 v16, 16, v9
	v_cndmask_b32_e64 v21, 0, v21, s[8:9]
	v_lshlrev_b32_e32 v25, 16, v13
	v_and_b32_e32 v9, 0xffff0000, v9
	v_cndmask_b32_e64 v17, 0, v17, s[8:9]
	v_and_b32_e32 v13, 0xffff0000, v13
	v_cndmask_b32_e64 v25, 0, v25, s[10:11]
	v_sub_f32_e32 v21, v21, v16
	v_cndmask_b32_e64 v13, 0, v13, s[10:11]
	v_sub_f32_e32 v17, v17, v9
	v_sub_f32_e32 v25, v25, v16
	v_fmac_f32_e32 v16, v21, v22
	s_waitcnt lgkmcnt(9)
	v_add_f32_e32 v21, -1.0, v76
	v_sub_f32_e32 v13, v13, v9
	v_fmac_f32_e32 v9, v17, v23
	v_fma_f32 v21, v42, v21, 1.0
	v_fmac_f32_e32 v9, v13, v27
	s_waitcnt lgkmcnt(7)
	v_add_f32_e32 v13, -1.0, v77
	v_fmac_f32_e32 v16, v25, v26
	v_mul_f32_e32 v21, v144, v21
	v_fma_f32 v13, v43, v13, 1.0
	v_mul_f32_e32 v22, v16, v21
	v_mul_f32_e32 v13, v143, v13
	v_fmac_f32_e32 v36, v38, v22
	v_mul_f32_e32 v17, v9, v13
	v_lshlrev_b32_e32 v22, 16, v18
	v_fmac_f32_e32 v36, v39, v17
	v_lshlrev_b32_e32 v17, 16, v10
	v_cndmask_b32_e64 v22, 0, v22, s[8:9]
	v_lshlrev_b32_e32 v23, 16, v14
	v_cndmask_b32_e64 v23, 0, v23, s[10:11]
	v_sub_f32_e32 v22, v22, v17
	v_sub_f32_e32 v23, v23, v17
	v_fmac_f32_e32 v17, v22, v0
	s_waitcnt lgkmcnt(5)
	v_add_f32_e32 v0, -1.0, v82
	v_fma_f32 v0, v32, v0, 1.0
	v_fmac_f32_e32 v17, v23, v4
	v_mul_f32_e32 v0, v141, v0
	v_mul_f32_e32 v4, v17, v0
	v_fmac_f32_e32 v36, v28, v4
	v_and_b32_e32 v4, 0xffff0000, v10
	v_and_b32_e32 v10, 0xffff0000, v18
	v_cndmask_b32_e64 v10, 0, v10, s[8:9]
	v_and_b32_e32 v14, 0xffff0000, v14
	v_cndmask_b32_e64 v14, 0, v14, s[10:11]
	v_sub_f32_e32 v10, v10, v4
	v_sub_f32_e32 v14, v14, v4
	v_fmac_f32_e32 v4, v10, v1
	s_waitcnt lgkmcnt(3)
	v_add_f32_e32 v1, -1.0, v83
	v_fma_f32 v1, v33, v1, 1.0
	v_fmac_f32_e32 v4, v14, v5
	v_mul_f32_e32 v1, v140, v1
	v_mul_f32_e32 v5, v4, v1
	v_lshlrev_b32_e32 v10, 16, v19
	v_fmac_f32_e32 v36, v29, v5
	v_lshlrev_b32_e32 v5, 16, v11
	v_cndmask_b32_e64 v10, 0, v10, s[8:9]
	v_lshlrev_b32_e32 v14, 16, v15
	v_cndmask_b32_e64 v14, 0, v14, s[10:11]
	v_sub_f32_e32 v10, v10, v5
	v_sub_f32_e32 v14, v14, v5
	v_fmac_f32_e32 v5, v10, v2
	v_fmac_f32_e32 v5, v14, v6
	s_waitcnt lgkmcnt(2)
	v_mul_f32_e32 v10, 0x3fb8aa3b, v84
	v_exp_f32_e32 v14, v85
	v_mul_f32_e32 v18, 0xbfb8aa3b, v84
	v_exp_f32_e32 v18, v18
	v_exp_f32_e32 v10, v10
	s_waitcnt lgkmcnt(1)
	v_add_f32_e32 v6, -1.0, v86
	v_mul_f32_e32 v2, v73, v24
	v_fma_f32 v6, v34, v6, 1.0
	v_mul_f32_e32 v6, v139, v6
	v_mul_f32_e64 v25, v14, -v2
	v_mul_f32_e32 v2, v2, v86
	v_mul_f32_e32 v26, v18, v2
	v_mul_f32_e32 v18, v18, v6
	v_mul_f32_e32 v27, v5, v10
	v_mul_f32_e32 v2, v5, v6
	v_mul_f32_e32 v5, 0x3fb8aa3b, v79
	v_exp_f32_e32 v6, v81
	v_mul_f32_e32 v10, 0xbfb8aa3b, v79
	v_exp_f32_e32 v10, v10
	v_exp_f32_e32 v5, v5
	v_fmac_f32_e32 v36, v30, v2
	v_mul_f32_e32 v2, v72, v24
	v_mul_f32_e64 v6, v6, -v2
	v_mul_f32_e32 v2, v2, v82
	v_mul_f32_e32 v14, v10, v2
	v_mul_f32_e32 v0, v10, v0
	v_mul_f32_e32 v5, v17, v5
	v_mul_f32_e32 v10, 0x3fb8aa3b, v80
	v_exp_f32_e32 v17, v78
	v_mul_f32_e32 v22, 0xbfb8aa3b, v80
	v_exp_f32_e32 v22, v22
	v_exp_f32_e32 v10, v10
	v_mul_f32_e32 v2, v70, v24
	v_mul_f32_e64 v17, v17, -v2
	v_mul_f32_e32 v2, v2, v83
	v_mul_f32_e32 v23, v22, v2
	v_mul_f32_e32 v4, v4, v10
	v_cvt_pk_bf16_f32 v2, v6, v17
	v_cvt_pk_bf16_f32 v6, v14, v23
	v_cvt_pk_bf16_f32 v14, v5, v4
	v_exp_f32_e32 v4, v75
	v_mul_f32_e32 v5, 0xbfb8aa3b, v71
	v_exp_f32_e32 v5, v5
	v_mul_f32_e32 v1, v22, v1
	v_cvt_pk_bf16_f32 v10, v0, v1
	v_mul_f32_e32 v0, v69, v24
	v_mul_f32_e32 v1, 0x3fb8aa3b, v71
	v_exp_f32_e32 v1, v1
	v_mul_f32_e64 v4, v4, -v0
	v_mul_f32_e32 v0, v0, v76
	v_mul_f32_e32 v0, v5, v0
	v_mul_f32_e32 v17, v5, v21
	v_mul_f32_e32 v5, 0x3fb8aa3b, v74
	v_exp_f32_e32 v21, v67
	v_mul_f32_e32 v22, 0xbfb8aa3b, v74
	v_exp_f32_e32 v22, v22
	v_exp_f32_e32 v5, v5
	v_mul_f32_e32 v16, v16, v1
	v_mul_f32_e32 v1, v68, v24
	v_mul_f32_e64 v21, v21, -v1
	v_mul_f32_e32 v1, v1, v77
	v_mul_f32_e32 v23, v22, v1
	v_mul_f32_e32 v13, v22, v13
	v_mul_f32_e32 v22, v9, v5
	v_cvt_pk_bf16_f32 v1, v4, v21
	v_cvt_pk_bf16_f32 v9, v17, v13
	v_cvt_pk_bf16_f32 v13, v16, v22
	v_mul_f32_e32 v4, 0x3fb8aa3b, v54
	v_exp_f32_e32 v16, v56
	v_mul_f32_e32 v17, 0xbfb8aa3b, v54
	v_exp_f32_e32 v17, v17
	v_exp_f32_e32 v4, v4
	v_cvt_pk_bf16_f32 v5, v0, v23
	v_mul_f32_e32 v0, v66, v24
	v_mul_f32_e64 v16, v16, -v0
	v_mul_f32_e32 v0, v0, v57
	v_mul_f32_e32 v23, 0xbfb8aa3b, v55
	v_mul_f32_e32 v21, v17, v0
	v_mul_f32_e32 v17, v17, v20
	v_mul_f32_e32 v20, v87, v4
	v_mul_f32_e32 v4, 0x3fb8aa3b, v55
	v_exp_f32_e32 v22, v53
	v_exp_f32_e32 v23, v23
	v_exp_f32_e32 v4, v4
	v_mul_f32_e32 v0, v65, v24
	v_mul_f32_e64 v22, v22, -v0
	v_mul_f32_e32 v0, v0, v58
	v_mul_f32_e32 v12, v23, v12
	v_mul_f32_e32 v28, v23, v0
	v_mul_f32_e32 v23, v8, v4
	v_cvt_pk_bf16_f32 v0, v16, v22
	v_cvt_pk_bf16_f32 v8, v17, v12
	v_and_b32_e32 v16, 0xffff0000, v19
	ds_read_b32 v17, v52 offset:28
	v_and_b32_e32 v11, 0xffff0000, v11
	v_cndmask_b32_e64 v16, 0, v16, s[8:9]
	v_and_b32_e32 v15, 0xffff0000, v15
	v_cndmask_b32_e64 v15, 0, v15, s[10:11]
	v_sub_f32_e32 v16, v16, v11
	v_sub_f32_e32 v15, v15, v11
	v_fmac_f32_e32 v11, v16, v3
	v_exp_f32_e32 v16, v59
	s_waitcnt lgkmcnt(1)
	v_mul_f32_e32 v19, 0xbfb8aa3b, v60
	v_exp_f32_e32 v19, v19
	v_fmac_f32_e32 v11, v15, v7
	s_waitcnt lgkmcnt(0)
	v_add_f32_e32 v7, -1.0, v17
	v_mul_f32_e32 v15, 0x3fb8aa3b, v60
	v_mul_f32_e32 v3, v64, v24
	v_fma_f32 v7, v35, v7, 1.0
	v_exp_f32_e32 v15, v15
	v_mul_f32_e32 v7, v138, v7
	v_mul_f32_e64 v16, v16, -v3
	v_mul_f32_e32 v3, v3, v17
	v_mul_f32_e32 v17, v19, v3
	v_mul_f32_e32 v3, v11, v7
	v_fmac_f32_e32 v36, v31, v3
	v_cvt_pk_bf16_f32 v3, v25, v16
	v_mul_lo_u32 v16, v48, s39
	v_mul_f32_e32 v19, v19, v7
	v_mul_f32_e32 v15, v11, v15
	v_add3_u32 v16, v111, v16, v104
	v_cvt_pk_bf16_f32 v4, v21, v28
	v_cvt_pk_bf16_f32 v12, v20, v23
	v_cvt_pk_bf16_f32 v20, v98, v95
	v_cvt_pk_bf16_f32 v21, v100, v99
	v_cvt_pk_bf16_f32 v22, v102, v101
	v_cvt_pk_bf16_f32 v23, v110, v61
	v_cvt_pk_bf16_f32 v7, v26, v17
	v_cvt_pk_bf16_f32 v11, v18, v19
	v_cvt_pk_bf16_f32 v15, v27, v15
	ds_write_b128 v16, v[0:3]
	ds_write_b128 v16, v[4:7] offset:18432
	ds_write_b128 v16, v[8:11] offset:36864
	ds_write_b128 v16, v[12:15] offset:55296
	ds_write_b128 v16, v[20:23] offset:64512
	v_add_f32_dpp v0, v36, v36 quad_perm:[1,0,3,2] row_mask:0xf bank_mask:0xf bound_ctrl:1
	v_cmp_eq_u32_e32 vcc, 0, v137
	s_nop 0
	v_add_f32_dpp v0, v0, v0 quad_perm:[2,3,0,1] row_mask:0xf bank_mask:0xf bound_ctrl:1
	s_nop 1
	v_mov_b32_dpp v1, v0 row_half_mirror row_mask:0xf bank_mask:0xf bound_ctrl:1
	s_and_saveexec_b64 s[0:1], vcc
	s_cbranch_execz .LBB0_426
	s_mul_i32 s28, s26, 0x2200
	v_lshl_add_u64 v[2:3], v[96:97], 0, s[28:29]
	v_readlane_b32 s8, v255, 10
	v_lshlrev_b64 v[2:3], 6, v[2:3]
	v_readlane_b32 s9, v255, 11
	v_add_f32_e32 v4, v0, v1
	s_lshl_b32 s28, s40, 2
	v_lshl_add_u64 v[0:1], s[8:9], 0, v[2:3]
	v_lshl_add_u64 v[0:1], v[0:1], 0, s[28:29]
	global_store_dword v[0:1], v4, off

.Lsub_rhs:
	ds_read_b64 v[0:1], v207
	ds_read_b128 v[224:227], v245 offset:2304
	ds_read_b128 v[246:249], v245 offset:4608
	ds_read_b128 v[216:219], v245 offset:6912
	ds_read_b128 v[220:223], v245 offset:6976
	v_mov_b32_e32 v2, v105
	v_mov_b32_e32 v3, v105
	v_mov_b32_e32 v104, v105
	v_cmp_gt_u32_e32 vcc, 16, v14
	s_waitcnt lgkmcnt(0)
	v_mov_b32_e32 v102, v208
	v_mov_b32_e32 v103, v209
	s_nop 1
	v_mfma_f32_16x16x32_bf16 v[26:29], v[0:3], v[102:105], 0
	ds_read_b64 v[0:1], v207 offset:768
	v_lshlrev_b32_e32 v18, 16, v210
	v_and_b32_e32 v19, 0xffff0000, v210
	v_lshlrev_b32_e32 v20, 16, v211
	v_and_b32_e32 v21, 0xffff0000, v211
	v_cndmask_b32_e32 v224, 0, v224, vcc
	v_cndmask_b32_e32 v225, 0, v225, vcc
	v_cndmask_b32_e32 v226, 0, v226, vcc
	v_cndmask_b32_e32 v227, 0, v227, vcc
	v_cvt_pk_bf16_f32 v22, v26, v27
	v_cvt_pk_bf16_f32 v23, v28, v29
	ds_write_b64 v24, v[22:23]
	ds_read_b128 v[14:17], v230
	s_waitcnt lgkmcnt(0)
	v_mfma_f32_16x16x32_bf16 v[18:21], v[224:227], v[14:17], v[18:21]
	v_cndmask_b32_e32 v220, 0, v220, vcc
	v_cndmask_b32_e32 v221, 0, v221, vcc
	v_cndmask_b32_e32 v222, 0, v222, vcc
	v_cndmask_b32_e32 v223, 0, v223, vcc
	s_nop 3
	v_cvt_pk_bf16_f32 v102, v18, v19
	v_cvt_pk_bf16_f32 v103, v20, v21
	s_nop 1
	v_mfma_f32_16x16x32_bf16 v[26:29], v[0:3], v[102:105], 0
	ds_read_b64 v[0:1], v207 offset:1536
	v_lshlrev_b32_e32 v18, 16, v228
	v_and_b32_e32 v19, 0xffff0000, v228
	v_lshlrev_b32_e32 v20, 16, v229
	v_and_b32_e32 v21, 0xffff0000, v229
	s_nop 3
	v_cvt_pk_bf16_f32 v22, v26, v27
	v_cvt_pk_bf16_f32 v23, v28, v29
	ds_write_b64 v24, v[22:23] offset:32
	ds_read_b128 v[14:17], v230
	s_waitcnt lgkmcnt(0)
	v_mfma_f32_16x16x32_bf16 v[18:21], v[246:249], v[14:17], v[18:21]
	s_nop 7
	v_cvt_pk_bf16_f32 v102, v18, v19
	v_cvt_pk_bf16_f32 v103, v20, v21
	s_nop 1
	v_mfma_f32_16x16x32_bf16 v[26:29], v[0:3], v[102:105], 0
	ds_read_b64 v[0:1], v207 offset:2304
	v_lshlrev_b32_e32 v18, 16, v250
	v_and_b32_e32 v19, 0xffff0000, v250
	v_lshlrev_b32_e32 v20, 16, v251
	v_and_b32_e32 v21, 0xffff0000, v251
	s_nop 3
	v_cvt_pk_bf16_f32 v22, v26, v27
	v_cvt_pk_bf16_f32 v23, v28, v29
	ds_write_b64 v24, v[22:23] offset:64
	ds_read_b128 v[14:17], v230
	ds_read_b128 v[224:227], v230 offset:64
	s_waitcnt lgkmcnt(0)
	v_mfma_f32_16x16x32_bf16 v[18:21], v[216:219], v[14:17], v[18:21]
	v_mfma_f32_16x16x32_bf16 v[18:21], v[220:223], v[224:227], v[18:21]
	s_nop 7
	v_cvt_pk_bf16_f32 v102, v18, v19
	v_cvt_pk_bf16_f32 v103, v20, v21
	s_nop 1
	v_mfma_f32_16x16x32_bf16 v[26:29], v[0:3], v[102:105], 0
	s_nop 7
	v_cvt_pk_bf16_f32 v22, v26, v27
	v_cvt_pk_bf16_f32 v23, v28, v29
	ds_write_b64 v24, v[22:23] offset:96
	s_branch .LBB0_380
.LBB0_449:
	v_and_b32_e32 v1, 48, v103
	s_branch .LBB0_430
